# lead the segment with resident reads, step 2: K-slot base and per-lane K read addresses computed before the loop-top waits/barrier so the first ds_reads issue right behind the barrier release; on top
# baseline (speedup 1.0000x reference)
.Lprio_skip_a1:
.LBB0_805:
	s_add_i32 s56, s12, -1
	s_waitcnt vmcnt(0)
	s_and_b32 s87, s56, 1
	s_mul_i32 s56, s87, 0x6000
	s_add_i32 s56, s56, 0
	s_add_i32 s56, s56, 0x8000
	v_add_u32_e32 v175, s56, v161
	v_add_u32_e32 v200, s56, v169
	v_add_u32_e32 v201, s56, v170
	s_cmp_ge_u32 s12, s85
	s_waitcnt vmcnt(0) lgkmcnt(0)
	s_barrier


.LBB0_807:


	ds_read_b128 v[66:69], v175 offset:0
	ds_read_b128 v[70:73], v175 offset:0x3000

	ds_read_b128 v[176:179], v200 offset:0
	ds_read_b128 v[180:183], v200 offset:0x3000

	ds_read_b128 v[184:187], v201 offset:0
	ds_read_b128 v[188:191], v201 offset:0x3000
	s_cmp_ge_u32 s12, s85
	s_cbranch_scc1 .Ldma_skip_a1
	s_xor_b32 s88, s87, 1
	s_mulk_i32 s88, 0x6000
	s_add_i32 s88, s64, s88
	s_add_i32 m0, s88, 0x8000
	s_nop 0
	global_load_lds_dwordx4 v244, s[94:95]
	s_add_i32 m0, s88, 0xa000
	s_nop 0
	global_load_lds_dwordx4 v243, s[94:95]
	s_add_i32 m0, s88, 0xc000
	s_lshl_b32 s88, s87, 14
	s_xor_b32 s88, s88, 0x4000
	s_add_i32 s88, s64, s88
	global_load_lds_dwordx4 v242, s[94:95]
	s_mov_b32 m0, s88
	s_nop 0
	global_load_lds_dwordx4 v241, s[96:97]
	s_add_i32 m0, s88, 0x2000
	s_nop 0
	global_load_lds_dwordx4 v240, s[96:97]

.Lprio_skip_a2:
.LBB0_946:
	s_add_i32 s44, s12, -1
	s_waitcnt vmcnt(0)
	s_and_b32 s48, s44, 1
	s_mul_i32 s44, s48, 0x6000
	s_add_i32 s44, s44, 0
	s_add_i32 s44, s44, 0x8000
	v_add_u32_e32 v177, s44, v171
	v_add_u32_e32 v206, s44, v172
	v_add_u32_e32 v207, s44, v173
	s_cmp_ge_u32 s12, s46
	s_waitcnt vmcnt(0) lgkmcnt(0)
	s_barrier


.LBB0_948:


	ds_read_b128 v[66:69], v177 offset:0
	ds_read_b128 v[82:85], v177 offset:0x3000

	ds_read_b128 v[178:181], v206 offset:0
	ds_read_b128 v[182:185], v206 offset:0x3000

	ds_read_b128 v[186:189], v207 offset:0
	ds_read_b128 v[190:193], v207 offset:0x3000
	s_cmp_ge_u32 s12, s46
	s_cbranch_scc1 .Ldma_skip_a2
	s_xor_b32 s88, s48, 1
	s_mulk_i32 s88, 0x6000
	s_add_i32 s88, s64, s88
	s_add_i32 m0, s88, 0x8000
	s_nop 0
	global_load_lds_dwordx4 v244, s[94:95]
	s_add_i32 m0, s88, 0xa000
	s_nop 0
	global_load_lds_dwordx4 v243, s[94:95]
	s_add_i32 m0, s88, 0xc000
	s_lshl_b32 s88, s48, 14
	s_xor_b32 s88, s88, 0x4000
	s_add_i32 s88, s64, s88
	global_load_lds_dwordx4 v242, s[94:95]
	s_mov_b32 m0, s88
	s_nop 0
	global_load_lds_dwordx4 v241, s[96:97]
	s_add_i32 m0, s88, 0x2000
	s_nop 0
	global_load_lds_dwordx4 v240, s[96:97]
